# v35: v34 + ph6 parts merge: part 1 of a group fetched together with part 0, next part fetched while the current one is merged
# baseline (speedup 1.0000x reference)
; __device__ __forceinline__ float rdl(float v, int l) { return __builtin_bit_cast(float, __builtin_amdgcn_readlane(__builtin_bit_cast(int, v), l)); }
; __device__ __forceinline__ void ph6_hf(const Frame& F, const Args& A) {
;     ...
;     for (int g = gw; g < S_; g += NGW) {
;         const int h = g & 7, row0 = (g >> 3) * 8, blk = h * 32 + (row0 >> 8), rr0 = row0 & 255;
;         const int np = __builtin_amdgcn_readfirstlane(NPART[blk]);
;         const float* pm = PML + (size_t)blk * MAXP * 512 + rr0 + mlo; const bf16* po = PO + (size_t)blk * MAXP * 32768 + (size_t)rr0 * 128 + 2 * lane;
;         unsigned gz[8], ov[8]; float M[8], L[8]; f32x2_t a[8];
;         { const float ml = pm[0];
; #pragma unroll
;           for (int q = 0; q < 8; ++q) { ov[q] = *(const unsigned*)(po + q * 128); gz[q] = *(const unsigned short*)(A.ws + WS_Z8 + (size_t)(row0 + q) * pg8::Z8LD + 1024 + h * 128 + 2 * lane); }
; #pragma unroll
;           for (int q = 0; q < 8; ++q) { M[q] = rdl(ml, q); L[q] = rdl(ml, 8 + q); a[q].x = bflo(ov[q]); a[q].y = bfhi(ov[q]); } }
.LBB0_972:
	s_ashr_i32 s20, s26, 8
	s_add_i32 s4, s20, s35
	s_ashr_i32 s5, s4, 31
	s_and_b32 s14, s26, -8
	s_and_b32 s10, s26, 0xf8
	s_lshl_b64 s[6:7], s[4:5], 2
	s_add_u32 s6, s31, s6
	s_addc_u32 s7, s33, s7
	global_load_dword v22, v35, s[6:7]
	s_lshl_b64 s[6:7], s[4:5], 15
	s_add_u32 s6, s29, s6
	s_addc_u32 s7, s30, s7
	s_lshl_b32 s8, s10, 2
	s_add_u32 s8, s6, s8
	s_addc_u32 s9, s7, 0
	s_lshl_b64 s[4:5], s[4:5], 20
	s_add_u32 s4, s27, s4
	s_addc_u32 s5, s28, s5
	s_lshl_b32 s6, s10, 8
	s_add_u32 s6, s4, s6
	s_addc_u32 s7, s5, 0
	s_mul_i32 s5, s14, 0x1800
	s_mul_hi_i32 s4, s14, 0x1800
	s_add_u32 s5, s88, s5
	global_load_dword v23, v1, s[8:9]
	global_load_dword v24, v42, s[6:7]
	s_addc_u32 s8, s89, s4
	s_add_u32 s4, s5, s36
	s_addc_u32 s5, s8, 0
	s_or_b32 s18, s14, 1
	v_lshl_add_u64 v[8:9], s[4:5], 0, v[34:35]
	s_mul_i32 s5, s18, 0x1800
	s_mul_hi_i32 s4, s18, 0x1800
	s_add_u32 s5, s88, s5
	s_addc_u32 s8, s89, s4
	s_add_u32 s4, s5, s36
	s_addc_u32 s5, s8, 0
	s_or_b32 s16, s14, 2
	v_lshl_add_u64 v[10:11], s[4:5], 0, v[34:35]
	s_mul_i32 s5, s16, 0x1800
	s_mul_hi_i32 s4, s16, 0x1800
	s_add_u32 s5, s88, s5
	s_addc_u32 s8, s89, s4
	s_add_u32 s4, s5, s36
	s_addc_u32 s5, s8, 0
	s_or_b32 s12, s14, 3
	v_lshl_add_u64 v[12:13], s[4:5], 0, v[34:35]
	s_mul_i32 s5, s12, 0x1800
	s_mul_hi_i32 s4, s12, 0x1800
	s_add_u32 s5, s88, s5
	s_addc_u32 s8, s89, s4
	s_add_u32 s4, s5, s36
	s_addc_u32 s5, s8, 0
	s_or_b32 s10, s14, 4
	v_lshl_add_u64 v[14:15], s[4:5], 0, v[34:35]
	s_mul_i32 s5, s10, 0x1800
	s_mul_hi_i32 s4, s10, 0x1800
	s_add_u32 s5, s88, s5
	s_addc_u32 s8, s89, s4
	s_add_u32 s4, s5, s36
	s_addc_u32 s5, s8, 0
	s_or_b32 s8, s14, 5
	v_add_co_u32_e32 v8, vcc, s37, v8
	v_lshl_add_u64 v[16:17], s[4:5], 0, v[34:35]
	s_mul_i32 s5, s8, 0x1800
	v_addc_co_u32_e32 v9, vcc, 0, v9, vcc
	s_mul_hi_i32 s4, s8, 0x1800
	s_add_u32 s5, s88, s5
	v_add_co_u32_e32 v10, vcc, s37, v10
	s_addc_u32 s9, s89, s4
	s_nop 0
	v_addc_co_u32_e32 v11, vcc, 0, v11, vcc
	s_add_u32 s4, s5, s36
	v_add_co_u32_e32 v12, vcc, s37, v12
	s_addc_u32 s5, s9, 0
	s_nop 0
	v_addc_co_u32_e32 v13, vcc, 0, v13, vcc
	v_lshl_add_u64 v[18:19], s[4:5], 0, v[34:35]
	s_or_b32 s4, s14, 6
	v_add_co_u32_e32 v14, vcc, s37, v14
	s_mul_i32 s9, s4, 0x1800
	s_nop 0
	v_addc_co_u32_e32 v15, vcc, 0, v15, vcc
	s_mul_hi_i32 s5, s4, 0x1800
	s_add_u32 s9, s88, s9
	v_add_co_u32_e32 v16, vcc, s37, v16
	s_addc_u32 s5, s89, s5
	s_nop 0
	v_addc_co_u32_e32 v17, vcc, 0, v17, vcc
	s_add_u32 s22, s9, s36
	v_add_co_u32_e32 v18, vcc, s37, v18
	s_addc_u32 s23, s5, 0
	s_nop 0
	v_addc_co_u32_e32 v19, vcc, 0, v19, vcc
	v_lshl_add_u64 v[20:21], s[22:23], 0, v[34:35]
	v_add_co_u32_e32 v20, vcc, s37, v20
	global_load_dword v25, v42, s[6:7] offset:256
	global_load_dword v27, v42, s[6:7] offset:512
	global_load_dword v30, v42, s[6:7] offset:768
	global_load_dword v31, v42, s[6:7] offset:1024
	global_load_dword v36, v42, s[6:7] offset:1280
	global_load_dword v37, v42, s[6:7] offset:1536
	v_addc_co_u32_e32 v21, vcc, 0, v21, vcc
	global_load_ushort v48, v[8:9], off offset:1024
	global_load_ushort v49, v[10:11], off offset:1024
	global_load_ushort v50, v[12:13], off offset:1024
	global_load_ushort v44, v[14:15], off offset:1024
	global_load_ushort v45, v[16:17], off offset:1024
	global_load_ushort v46, v[18:19], off offset:1024
	global_load_ushort v43, v[20:21], off offset:1024
	global_load_dword v10, v42, s[6:7] offset:1792
	s_or_b32 s6, s26, 7
	s_mul_i32 s7, s6, 0x1800
	s_mul_hi_i32 s5, s6, 0x1800
	s_add_u32 s7, s88, s7
	s_addc_u32 s5, s89, s5
	s_add_u32 s22, s7, s36
	s_addc_u32 s23, s5, 0
	v_lshl_add_u64 v[8:9], s[22:23], 0, v[34:35]
	v_add_co_u32_e32 v8, vcc, s37, v8
	s_nop 1
	v_addc_co_u32_e32 v9, vcc, 0, v9, vcc
	global_load_ushort v47, v[8:9], off offset:1024
	s_lshl_b32 s98, s20, 15
	s_lshl_b32 s99, s26, 2
	s_and_b32 s99, s99, 0x3e0
	s_or_b32 s98, s98, s99
	s_mov_b32 s99, 0
	v_lshl_add_u64 v[210:211], v[4:5], 0, s[98:99]
	s_lshl_b32 s98, s20, 20
	s_lshl_b32 s99, s26, 8
	s_and_b32 s99, s99, 0xf800
	s_or_b32 s98, s98, s99
	s_mov_b32 s99, 0
	v_lshl_add_u64 v[212:213], v[6:7], 0, s[98:99]
	global_load_dword v200, v[210:211], off
	global_load_dword v201, v[212:213], off offset:-1024
	global_load_dword v202, v[212:213], off offset:-768
	global_load_dword v203, v[212:213], off offset:-512
	global_load_dword v204, v[212:213], off offset:-256
	global_load_dword v205, v[212:213], off
	global_load_dword v206, v[212:213], off offset:256
	global_load_dword v207, v[212:213], off offset:512
	global_load_dword v208, v[212:213], off offset:768
	s_waitcnt vmcnt(0)
	v_readfirstlane_b32 s5, v22
	v_readlane_b32 s7, v23, 0
	v_readlane_b32 s11, v23, 8
	v_lshlrev_b32_e32 v32, 16, v24
	v_and_b32_e32 v33, 0xffff0000, v24
	v_readlane_b32 s9, v23, 1
	v_readlane_b32 s15, v23, 9
	v_readlane_b32 s13, v23, 2
	v_readlane_b32 s19, v23, 10
	v_readlane_b32 s17, v23, 3
	v_readlane_b32 s23, v23, 11
	v_readlane_b32 s22, v23, 4
	v_readlane_b32 s25, v23, 12
	v_readlane_b32 s24, v23, 5
	v_readlane_b32 s39, v23, 13
	v_readlane_b32 s38, v23, 6
	v_readlane_b32 s41, v23, 14
	v_readlane_b32 s40, v23, 7
	v_readlane_b32 s42, v23, 15
	s_cmp_lt_i32 s5, 2
	v_lshlrev_b32_e32 v28, 16, v25
	v_and_b32_e32 v29, 0xffff0000, v25
	v_lshlrev_b32_e32 v26, 16, v27
	v_and_b32_e32 v27, 0xffff0000, v27
	v_lshlrev_b32_e32 v24, 16, v30
	v_and_b32_e32 v25, 0xffff0000, v30
	v_lshlrev_b32_e32 v18, 16, v31
	v_and_b32_e32 v19, 0xffff0000, v31
	v_lshlrev_b32_e32 v16, 16, v36
	v_and_b32_e32 v17, 0xffff0000, v36
	v_lshlrev_b32_e32 v12, 16, v37
	v_and_b32_e32 v13, 0xffff0000, v37
	v_lshlrev_b32_e32 v8, 16, v10
	v_and_b32_e32 v10, 0xffff0000, v10
	s_cbranch_scc1 .LBB0_970
	s_lshl_b32 s21, s26, 2
	s_and_b32 s43, s21, 0x3e0
	s_lshl_b32 s21, s26, 8
	s_and_b32 s46, s21, 0xf800
	s_ashr_i32 s21, s20, 31
	s_lshl_b64 s[44:45], s[20:21], 15
	s_lshl_b64 s[20:21], s[20:21], 20
	s_or_b32 s44, s44, s43
	s_or_b32 s20, s20, s46
	s_add_i32 s5, s5, -1
	v_lshl_add_u64 v[38:39], v[4:5], 0, s[44:45]
	v_lshl_add_u64 v[40:41], v[6:7], 0, s[20:21]
	v_mov_b32_e32 v14, s42
	v_mov_b32_e32 v20, s41
	v_mov_b32_e32 v23, s39
	v_mov_b32_e32 v22, s25
	v_mov_b32_e32 v31, s23
	v_mov_b32_e32 v30, s19
	v_mov_b32_e32 v37, s15
	v_mov_b32_e32 v36, s11
	v_mov_b32_e32 v51, s40
	v_mov_b32_e32 v52, s38
	v_mov_b32_e32 v53, s24
	v_mov_b32_e32 v54, s22
	v_mov_b32_e32 v55, s17
	v_mov_b32_e32 v56, s13
	v_mov_b32_e32 v57, s9
	v_mov_b32_e32 v58, s7
; __device__ __forceinline__ float rdl(float v, int l) { return __builtin_bit_cast(float, __builtin_amdgcn_readlane(__builtin_bit_cast(int, v), l)); }
; __device__ __forceinline__ void ph6_hf(const Frame& F, const Args& A) {
;     ...
;         for (int p = 1; p < np; ++p) { const float ml = pm[(size_t)p * 512];
; #pragma unroll
;             for (int q = 0; q < 8; ++q) ov[q] = *(const unsigned*)(po + (size_t)p * 32768 + q * 128);
; #pragma unroll
;             for (int q = 0; q < 8; ++q) { const float mp = rdl(ml, q), lp = rdl(ml, 8 + q);
;                 const float Mn = fmaxf(M[q], mp), w0 = __builtin_amdgcn_exp2f((M[q] - Mn) * C2), w1 = __builtin_amdgcn_exp2f((mp - Mn) * C2);
;                 L[q] = L[q] * w0 + lp * w1; a[q].x = a[q].x * w0 + bflo(ov[q]) * w1; a[q].y = a[q].y * w0 + bfhi(ov[q]) * w1; M[q] = Mn; } }
.LBB0_974:
	s_waitcnt vmcnt(0)
	v_mov_b32_e32 v9, v200
	v_mov_b32_e32 v11, v201
	v_mov_b32_e32 v15, v202
	v_mov_b32_e32 v21, v203
	v_mov_b32_e32 v59, v204
	v_mov_b32_e32 v69, v205
	v_mov_b32_e32 v71, v206
	v_mov_b32_e32 v73, v207
	v_mov_b32_e32 v74, v208
	v_max_f32_e32 v75, v58, v58
	v_max_f32_e32 v76, v57, v57
	v_max_f32_e32 v77, v56, v56
	v_max_f32_e32 v79, v54, v54
	v_max_f32_e32 v78, v55, v55
	v_max_f32_e32 v80, v53, v53
	v_max_f32_e32 v81, v52, v52
	v_max_f32_e32 v82, v51, v51
	s_add_i32 s5, s5, -1
	v_lshl_add_u64 v[38:39], v[38:39], 0, s[0:1]
	v_lshl_add_u64 v[40:41], v[40:41], 0, s[2:3]
	s_cmp_eq_u32 s5, 0
	global_load_dword v200, v[38:39], off
	global_load_dword v201, v[40:41], off offset:-1024
	global_load_dword v202, v[40:41], off offset:-768
	global_load_dword v203, v[40:41], off offset:-512
	global_load_dword v204, v[40:41], off offset:-256
	global_load_dword v205, v[40:41], off
	global_load_dword v206, v[40:41], off offset:256
	global_load_dword v207, v[40:41], off offset:512
	global_load_dword v208, v[40:41], off offset:768
	v_readlane_b32 s7, v9, 0
	v_readlane_b32 s9, v9, 1
	v_readlane_b32 s11, v9, 2
	v_readlane_b32 s15, v9, 4
	v_readlane_b32 s20, v9, 8
	v_lshlrev_b32_e32 v60, 16, v11
	v_and_b32_e32 v61, 0xffff0000, v11
	v_readlane_b32 s21, v9, 9
	v_readlane_b32 s22, v9, 10
	v_lshlrev_b32_e32 v64, 16, v21
	v_and_b32_e32 v65, 0xffff0000, v21
	v_readlane_b32 s13, v9, 3
	v_readlane_b32 s23, v9, 11
	v_lshlrev_b32_e32 v66, 16, v59
	v_and_b32_e32 v67, 0xffff0000, v59
	v_readlane_b32 s24, v9, 12
	v_readlane_b32 s17, v9, 5
	v_readlane_b32 s25, v9, 13
	v_readlane_b32 s19, v9, 6
	v_readlane_b32 s38, v9, 14
	v_readlane_b32 s39, v9, 7
	v_readlane_b32 s40, v9, 15
	v_lshlrev_b32_e32 v9, 16, v74
	v_and_b32_e32 v21, 0xffff0000, v74
	v_max_f32_e64 v11, s7, s7
	v_max_f32_e64 v59, s9, s9
	v_max_f32_e64 v74, s11, s11
	v_max_f32_e64 v84, s15, s15
	v_max_f32_e64 v83, s13, s13
	v_max_f32_e64 v85, s17, s17
	v_max_f32_e64 v86, s19, s19
	v_max_f32_e64 v87, s39, s39
	v_max_f32_e32 v11, v75, v11
	v_max_f32_e32 v59, v76, v59
	v_max_f32_e32 v74, v77, v74
	v_max_f32_e32 v76, v79, v84
	v_max_f32_e32 v75, v78, v83
	v_max_f32_e32 v77, v80, v85
	v_max_f32_e32 v78, v81, v86
	v_max_f32_e32 v79, v82, v87
	v_sub_f32_e32 v81, s7, v11
	v_sub_f32_e32 v83, s9, v59
	v_sub_f32_e32 v85, s11, v74
	v_sub_f32_e32 v89, s15, v76
	v_sub_f32_e32 v80, v58, v11
	v_sub_f32_e32 v82, v57, v59
	v_sub_f32_e32 v84, v56, v74
	v_sub_f32_e32 v90, v53, v77
	v_sub_f32_e32 v91, s17, v77
	v_sub_f32_e32 v94, v51, v79
	v_sub_f32_e32 v95, s39, v79
	v_mov_b32_e32 v51, v79
	v_mov_b32_e32 v53, v77
	v_mov_b32_e32 v57, v59
	v_mul_f32_e32 v59, 0x3e0293ee, v81
	v_mul_f32_e32 v77, 0x3e0293ee, v83
	v_mul_f32_e32 v79, 0x3e0293ee, v85
	v_mul_f32_e32 v83, 0x3e0293ee, v89
	v_sub_f32_e32 v86, v55, v75
	v_sub_f32_e32 v87, s13, v75
	v_sub_f32_e32 v88, v54, v76
	v_sub_f32_e32 v92, v52, v78
	v_sub_f32_e32 v93, s19, v78
	v_mov_b32_e32 v52, v78
	v_mov_b32_e32 v54, v76
	v_mov_b32_e32 v58, v11
	v_mul_f32_e32 v11, 0x3e0293ee, v80
	v_mul_f32_e32 v78, 0x3e0293ee, v84
	v_exp_f32_e32 v76, v59
	v_exp_f32_e32 v80, v79
	v_exp_f32_e32 v84, v83
	v_mov_b32_e32 v55, v75
	v_mul_f32_e32 v75, 0x3e0293ee, v82
	v_mul_f32_e32 v81, 0x3e0293ee, v86
	v_mul_f32_e32 v85, 0x3e0293ee, v87
	v_mul_f32_e32 v82, 0x3e0293ee, v88
	v_mul_f32_e32 v86, 0x3e0293ee, v90
	v_mul_f32_e32 v87, 0x3e0293ee, v91
	v_mul_f32_e32 v88, 0x3e0293ee, v92
	v_mul_f32_e32 v89, 0x3e0293ee, v93
	v_mul_f32_e32 v90, 0x3e0293ee, v94
	v_mul_f32_e32 v91, 0x3e0293ee, v95
	v_exp_f32_e32 v83, v86
	v_exp_f32_e32 v86, v88
	v_exp_f32_e32 v88, v89
	v_exp_f32_e32 v90, v90
	v_exp_f32_e32 v91, v91
	v_lshlrev_b32_e32 v68, 16, v69
	v_and_b32_e32 v69, 0xffff0000, v69
	v_exp_f32_e32 v78, v78
	v_exp_f32_e32 v79, v81
	v_exp_f32_e32 v82, v82
	v_pk_mul_f32 v[60:61], v[76:77], v[60:61] op_sel_hi:[0,1]
	v_exp_f32_e32 v77, v77
	v_pk_mul_f32 v[64:65], v[80:81], v[64:65] op_sel_hi:[0,1]
	v_exp_f32_e32 v81, v85
	v_pk_mul_f32 v[68:69], v[84:85], v[68:69] op_sel_hi:[0,1]
	v_exp_f32_e32 v85, v87
	v_lshlrev_b32_e32 v62, 16, v15
	v_and_b32_e32 v63, 0xffff0000, v15
	v_lshlrev_b32_e32 v72, 16, v73
	v_and_b32_e32 v73, 0xffff0000, v73
	v_mov_b32_e32 v15, s40
	v_mov_b32_e32 v56, v74
	v_exp_f32_e32 v74, v11
	v_exp_f32_e32 v75, v75
	v_mul_f32_e32 v98, s38, v88
	v_pk_mul_f32 v[72:73], v[88:89], v[72:73] op_sel_hi:[0,1]
	v_pk_mul_f32 v[14:15], v[14:15], v[90:91]
	v_mul_f32_e32 v88, v91, v9
	v_mov_b32_e32 v11, v91
	v_mov_b32_e32 v91, v21
	v_pk_mul_f32 v[10:11], v[10:11], v[90:91]
	v_lshlrev_b32_e32 v70, 16, v71
	v_and_b32_e32 v71, 0xffff0000, v71
	v_mul_f32_e32 v20, v20, v86
	v_mul_f32_e32 v8, v8, v90
	v_mov_b32_e32 v21, v14
	v_mov_b32_e32 v99, v15
	v_pk_fma_f32 v[26:27], v[26:27], v[78:79], v[64:65] op_sel_hi:[1,0,1]
	v_pk_fma_f32 v[18:19], v[18:19], v[82:83], v[68:69] op_sel_hi:[1,0,1]
	v_pk_fma_f32 v[12:13], v[12:13], v[86:87], v[72:73] op_sel_hi:[1,0,1]
	v_mov_b32_e32 v9, v10
	v_mov_b32_e32 v89, v11
	v_mov_b32_e32 v64, v77
	v_pk_mul_f32 v[68:69], s[22:23], v[80:81]
	v_mov_b32_e32 v72, v81
	v_mov_b32_e32 v80, v85
	v_mov_b32_e32 v92, v75
	v_mov_b32_e32 v94, v79
	v_mov_b32_e32 v96, v83
	v_pk_fma_f32 v[32:33], v[32:33], v[74:75], v[60:61] op_sel_hi:[1,0,1]
	v_pk_add_f32 v[20:21], v[20:21], v[98:99]
	v_pk_add_f32 v[8:9], v[8:9], v[88:89]
	v_pk_mul_f32 v[60:61], s[20:21], v[76:77]
	v_pk_mul_f32 v[76:77], s[24:25], v[84:85]
	v_pk_mul_f32 v[62:63], v[64:65], v[62:63] op_sel_hi:[0,1]
	v_pk_mul_f32 v[64:65], v[72:73], v[66:67] op_sel_hi:[0,1]
	v_pk_mul_f32 v[66:67], v[80:81], v[70:71] op_sel_hi:[0,1]
	v_mov_b32_e32 v14, v21
	v_mov_b32_e32 v10, v9
	v_pk_fma_f32 v[36:37], v[36:37], v[74:75], v[60:61]
	v_pk_fma_f32 v[30:31], v[30:31], v[78:79], v[68:69]
	v_pk_fma_f32 v[22:23], v[22:23], v[82:83], v[76:77]
	v_pk_fma_f32 v[28:29], v[28:29], v[92:93], v[62:63] op_sel_hi:[1,0,1]
	v_pk_fma_f32 v[24:25], v[24:25], v[94:95], v[64:65] op_sel_hi:[1,0,1]
	v_pk_fma_f32 v[16:17], v[16:17], v[96:97], v[66:67] op_sel_hi:[1,0,1]
	s_cbranch_scc0 .LBB0_974
	s_branch .LBB0_971
